# attention epilogue: eight 8-byte row-piece stores per lane widened to four 16-byte stores via v_permlane32_swap (on top of ticket prefetch)
# baseline (speedup 1.0000x reference)
.LBB0_950:
	s_waitcnt vmcnt(0)
	v_readfirstlane_b32 s38, v241
	v_mov_b32_e32 v48, v173
	s_nop 1
	v_permlane32_swap_b32_e32 v173, v48
	v_add_f32_e32 v48, v173, v48
	v_div_scale_f32 v49, s[14:15], v48, v48, 1.0
	v_rcp_f32_e32 v50, v49
	s_lshl_b32 s64, s23, 7
	v_lshlrev_b32_e32 v208, 2, v188
	s_mov_b64 s[14:15], 0x23c00200
	v_fma_f32 v51, -v49, v50, 1.0
	v_fmac_f32_e32 v50, v51, v50
	v_div_scale_f32 v51, vcc, 1.0, v48, 1.0
	v_mul_f32_e32 v52, v51, v50
	v_fma_f32 v53, -v49, v52, v51
	v_fmac_f32_e32 v52, v53, v50
	v_fma_f32 v49, -v49, v52, v51
	v_div_fmas_f32 v49, v49, v50, v52
	v_lshlrev_b64 v[50:51], 11, v[200:201]
	v_lshl_add_u64 v[50:51], s[8:9], 0, v[50:51]
	v_lshl_add_u64 v[50:51], v[50:51], 0, s[64:65]
	v_div_fixup_f32 v48, v49, v48, 1.0
	v_lshl_add_u64 v[50:51], v[50:51], 0, v[208:209]
	v_lshl_add_u64 v[52:53], v[50:51], 0, s[14:15]
	v_pk_mul_f32 v[32:33], v[32:33], v[48:49] op_sel_hi:[1,0]
	v_pk_mul_f32 v[34:35], v[34:35], v[48:49] op_sel_hi:[1,0]
	v_pk_mul_f32 v[36:37], v[36:37], v[48:49] op_sel_hi:[1,0]
	v_pk_mul_f32 v[38:39], v[38:39], v[48:49] op_sel_hi:[1,0]
	v_cvt_pk_bf16_f32 v32, v32, v33
	v_cvt_pk_bf16_f32 v33, v34, v35
	v_cvt_pk_bf16_f32 v34, v36, v37
	v_cvt_pk_bf16_f32 v35, v38, v39
	v_pk_mul_f32 v[16:17], v[16:17], v[48:49] op_sel_hi:[1,0]
	v_pk_mul_f32 v[18:19], v[18:19], v[48:49] op_sel_hi:[1,0]
	v_pk_mul_f32 v[20:21], v[20:21], v[48:49] op_sel_hi:[1,0]
	v_pk_mul_f32 v[22:23], v[22:23], v[48:49] op_sel_hi:[1,0]
	v_cvt_pk_bf16_f32 v16, v16, v17
	v_cvt_pk_bf16_f32 v17, v18, v19
	v_cvt_pk_bf16_f32 v18, v20, v21
	v_cvt_pk_bf16_f32 v19, v22, v23
	v_permlane32_swap_b32_e32 v32, v34
	v_permlane32_swap_b32_e32 v33, v35
	global_store_dwordx4 v[52:53], v[32:35], off
	v_pk_mul_f32 v[40:41], v[40:41], v[48:49] op_sel_hi:[1,0]
	v_pk_mul_f32 v[42:43], v[42:43], v[48:49] op_sel_hi:[1,0]
	v_pk_mul_f32 v[44:45], v[44:45], v[48:49] op_sel_hi:[1,0]
	v_pk_mul_f32 v[46:47], v[46:47], v[48:49] op_sel_hi:[1,0]
	v_cvt_pk_bf16_f32 v40, v40, v41
	v_cvt_pk_bf16_f32 v41, v42, v43
	v_cvt_pk_bf16_f32 v42, v44, v45
	v_cvt_pk_bf16_f32 v43, v46, v47
	v_permlane32_swap_b32_e32 v16, v18
	v_permlane32_swap_b32_e32 v17, v19
	global_store_dwordx4 v[52:53], v[16:19], off offset:64
	v_pk_mul_f32 v[24:25], v[24:25], v[48:49] op_sel_hi:[1,0]
	v_pk_mul_f32 v[26:27], v[26:27], v[48:49] op_sel_hi:[1,0]
	v_pk_mul_f32 v[28:29], v[28:29], v[48:49] op_sel_hi:[1,0]
	v_pk_mul_f32 v[30:31], v[30:31], v[48:49] op_sel_hi:[1,0]
	v_cvt_pk_bf16_f32 v24, v24, v25
	v_cvt_pk_bf16_f32 v25, v26, v27
	v_cvt_pk_bf16_f32 v26, v28, v29
	v_cvt_pk_bf16_f32 v27, v30, v31
	v_permlane32_swap_b32_e32 v40, v42
	v_permlane32_swap_b32_e32 v41, v43
	global_store_dwordx4 v[52:53], v[40:43], off offset:32
	s_mov_b64 s[14:15], 0
	s_nop 1
	v_permlane32_swap_b32_e32 v24, v26
	v_permlane32_swap_b32_e32 v25, v27
	global_store_dwordx4 v[52:53], v[24:27], off offset:96
